# rec gates: MFMA accumulators in VGPRs (no accvgpr reads), packed f32 ops replaced by scalar fma/mul/add; flags written before next-step poll issue; pconv2 Y stores write-through
# baseline (speedup 1.0000x reference)
.Lr0_rdy:
	v_lshl_add_u32 v66, s54, 11, v1
	ds_read_b128 v[118:121], v66
	ds_read_b128 v[122:125], v66 offset:1024
	s_cmp_eq_u32 s54, 0
	s_cbranch_scc1 .Lr0_first
	global_load_dwordx4 v[164:167], v[196:197], off nt
	global_load_dwordx4 v[168:171], v[196:197], off offset:1024 nt
	global_load_dwordx4 v[172:175], v[196:197], off offset:2048 nt
	global_load_dwordx4 v[176:179], v[196:197], off offset:3072 nt
	global_load_dwordx4 v[180:183], v[198:199], off nt
	global_load_dwordx4 v[184:187], v[198:199], off offset:1024 nt
	global_load_dwordx4 v[188:191], v[198:199], off offset:2048 nt
	global_load_dwordx4 v[192:195], v[198:199], off offset:3072 nt
	s_mov_b32 s55, 0
	s_waitcnt lgkmcnt(0)
.Lr0_consA:
	s_waitcnt vmcnt(15)
	v_mfma_f32_16x16x32_f16 v[66:69], v[58:61], v[132:135], v[118:121]
	v_max_u32_e32 v206, v133, v135
	v_mfma_f32_16x16x32_f16 v[70:73], v[26:29], v[132:135], v[122:125]
	s_waitcnt vmcnt(14)
	v_mfma_f32_16x16x32_f16 v[66:69], v[2:5], v[136:139], v[66:69]
	v_max3_u32 v206, v137, v139, v206
	v_mfma_f32_16x16x32_f16 v[70:73], v[30:33], v[136:139], v[70:73]
	s_waitcnt vmcnt(13)
	v_mfma_f32_16x16x32_f16 v[66:69], v[6:9], v[140:143], v[66:69]
	v_max3_u32 v206, v141, v143, v206
	v_mfma_f32_16x16x32_f16 v[70:73], v[34:37], v[140:143], v[70:73]
	s_waitcnt vmcnt(12)
	v_mfma_f32_16x16x32_f16 v[66:69], v[10:13], v[144:147], v[66:69]
	v_max3_u32 v206, v145, v147, v206
	v_mfma_f32_16x16x32_f16 v[70:73], v[38:41], v[144:147], v[70:73]
	s_waitcnt vmcnt(11)
	v_mfma_f32_16x16x32_f16 v[66:69], v[14:17], v[148:151], v[66:69]
	v_max3_u32 v206, v149, v151, v206
	v_mfma_f32_16x16x32_f16 v[70:73], v[46:49], v[148:151], v[70:73]
	s_waitcnt vmcnt(10)
	v_mfma_f32_16x16x32_f16 v[66:69], v[18:21], v[152:155], v[66:69]
	v_max3_u32 v206, v153, v155, v206
	v_mfma_f32_16x16x32_f16 v[70:73], v[50:53], v[152:155], v[70:73]
	s_waitcnt vmcnt(9)
	v_mfma_f32_16x16x32_f16 v[66:69], v[22:25], v[156:159], v[66:69]
	v_max3_u32 v206, v157, v159, v206
	v_mfma_f32_16x16x32_f16 v[70:73], v[54:57], v[156:159], v[70:73]
	s_waitcnt vmcnt(8)
	v_mfma_f32_16x16x32_f16 v[66:69], v[42:45], v[160:163], v[66:69]
	v_max3_u32 v206, v161, v163, v206
	v_mfma_f32_16x16x32_f16 v[70:73], v[62:65], v[160:163], v[70:73]
	v_cmp_lt_u32_e32 vcc, s59, v206
	s_cbranch_vccz .Lr0_gates
	s_add_i32 s55, s55, 1
	s_and_b32 s60, s55, 7
	s_cmp_eq_u32 s60, 7
	s_cbranch_scc1 .Lr0_reA_sc1
	global_load_dwordx4 v[132:135], v[196:197], off nt
	global_load_dwordx4 v[136:139], v[196:197], off offset:1024 nt
	global_load_dwordx4 v[140:143], v[196:197], off offset:2048 nt
	global_load_dwordx4 v[144:147], v[196:197], off offset:3072 nt
	global_load_dwordx4 v[148:151], v[198:199], off nt
	global_load_dwordx4 v[152:155], v[198:199], off offset:1024 nt
	global_load_dwordx4 v[156:159], v[198:199], off offset:2048 nt
	global_load_dwordx4 v[160:163], v[198:199], off offset:3072 nt
	s_branch .Lr0_consB

.Lr0_consB:
	s_waitcnt vmcnt(15)
	v_mfma_f32_16x16x32_f16 v[66:69], v[58:61], v[164:167], v[118:121]
	v_max_u32_e32 v206, v165, v167
	v_mfma_f32_16x16x32_f16 v[70:73], v[26:29], v[164:167], v[122:125]
	s_waitcnt vmcnt(14)
	v_mfma_f32_16x16x32_f16 v[66:69], v[2:5], v[168:171], v[66:69]
	v_max3_u32 v206, v169, v171, v206
	v_mfma_f32_16x16x32_f16 v[70:73], v[30:33], v[168:171], v[70:73]
	s_waitcnt vmcnt(13)
	v_mfma_f32_16x16x32_f16 v[66:69], v[6:9], v[172:175], v[66:69]
	v_max3_u32 v206, v173, v175, v206
	v_mfma_f32_16x16x32_f16 v[70:73], v[34:37], v[172:175], v[70:73]
	s_waitcnt vmcnt(12)
	v_mfma_f32_16x16x32_f16 v[66:69], v[10:13], v[176:179], v[66:69]
	v_max3_u32 v206, v177, v179, v206
	v_mfma_f32_16x16x32_f16 v[70:73], v[38:41], v[176:179], v[70:73]
	s_waitcnt vmcnt(11)
	v_mfma_f32_16x16x32_f16 v[66:69], v[14:17], v[180:183], v[66:69]
	v_max3_u32 v206, v181, v183, v206
	v_mfma_f32_16x16x32_f16 v[70:73], v[46:49], v[180:183], v[70:73]
	s_waitcnt vmcnt(10)
	v_mfma_f32_16x16x32_f16 v[66:69], v[18:21], v[184:187], v[66:69]
	v_max3_u32 v206, v185, v187, v206
	v_mfma_f32_16x16x32_f16 v[70:73], v[50:53], v[184:187], v[70:73]
	s_waitcnt vmcnt(9)
	v_mfma_f32_16x16x32_f16 v[66:69], v[22:25], v[188:191], v[66:69]
	v_max3_u32 v206, v189, v191, v206
	v_mfma_f32_16x16x32_f16 v[70:73], v[54:57], v[188:191], v[70:73]
	s_waitcnt vmcnt(8)
	v_mfma_f32_16x16x32_f16 v[66:69], v[42:45], v[192:195], v[66:69]
	v_max3_u32 v206, v193, v195, v206
	v_mfma_f32_16x16x32_f16 v[70:73], v[62:65], v[192:195], v[70:73]
	v_cmp_lt_u32_e32 vcc, s59, v206
	s_cbranch_vccz .Lr0_gates
	s_cmp_gt_u32 s55, 0xfffff
	s_cbranch_scc1 .Lr0_gates
	global_load_dwordx4 v[164:167], v[196:197], off nt
	global_load_dwordx4 v[168:171], v[196:197], off offset:1024 nt
	global_load_dwordx4 v[172:175], v[196:197], off offset:2048 nt
	global_load_dwordx4 v[176:179], v[196:197], off offset:3072 nt
	global_load_dwordx4 v[180:183], v[198:199], off nt
	global_load_dwordx4 v[184:187], v[198:199], off offset:1024 nt
	global_load_dwordx4 v[188:191], v[198:199], off offset:2048 nt
	global_load_dwordx4 v[192:195], v[198:199], off offset:3072 nt
	s_branch .Lr0_consA
.Lr0_first:
	s_waitcnt lgkmcnt(0)
	v_mov_b32_e32 v66, v118
	v_mov_b32_e32 v67, v119
	v_mov_b32_e32 v68, v120
	v_mov_b32_e32 v69, v121
	v_mov_b32_e32 v70, v122
	v_mov_b32_e32 v71, v123
	v_mov_b32_e32 v72, v124
	v_mov_b32_e32 v73, v125
.Lr0_gates:
	s_lshl_b32 s60, s58, 13
	s_mov_b32 s61, 0
	v_lshl_add_u64 v[196:197], v[196:197], 0, s[56:57]
	v_lshl_add_u64 v[198:199], v[198:199], 0, s[56:57]
	v_lshl_add_u64 v[200:201], v[200:201], 0, s[56:57]
	v_lshl_add_u64 v[202:203], v[202:203], 0, s[56:57]
	v_lshl_add_u64 v[204:205], v[108:109], 0, s[60:61]
	v_exp_f32_e32 v66, v66
	v_exp_f32_e32 v67, v67
	v_exp_f32_e32 v68, v68
	v_exp_f32_e32 v69, v69
	v_exp_f32_e32 v70, v70
	v_exp_f32_e32 v71, v71
	v_exp_f32_e32 v72, v72
	v_exp_f32_e32 v73, v73
	v_add_f32_e32 v66, 1.0, v66
	v_add_f32_e32 v67, 1.0, v67
	v_add_f32_e32 v68, 1.0, v68
	v_add_f32_e32 v69, 1.0, v69
	v_add_f32_e32 v70, 1.0, v70
	v_add_f32_e32 v71, 1.0, v71
	v_add_f32_e32 v72, 1.0, v72
	v_add_f32_e32 v73, 1.0, v73
	v_rcp_f32_e32 v70, v70
	v_rcp_f32_e32 v71, v71
	v_rcp_f32_e32 v72, v72
	v_rcp_f32_e32 v73, v73
	v_rcp_f32_e32 v74, v66
	v_rcp_f32_e32 v75, v67
	v_rcp_f32_e32 v76, v68
	v_rcp_f32_e32 v77, v69
	v_fma_f32 v70, v100, v70, v102
	v_fma_f32 v71, v100, v71, v102
	v_fma_f32 v72, v100, v72, v102
	v_fma_f32 v73, v100, v73, v102
	v_mul_f32_e32 v78, v74, v70
	v_mul_f32_e32 v79, v75, v71
	v_mul_f32_e32 v80, v76, v72
	v_mul_f32_e32 v81, v77, v73
	v_mov_b32_e32 v82, v78
	v_mov_b32_e32 v83, v79
	v_mov_b32_e32 v84, v80
	v_mov_b32_e32 v85, v81
	v_permlane32_swap_b32_e32 v78, v82
	v_permlane32_swap_b32_e32 v79, v83
	v_permlane32_swap_b32_e32 v80, v84
	v_permlane32_swap_b32_e32 v81, v85
	v_fma_f32 v112, v112, v74, v78
	v_fma_f32 v113, v113, v75, v79
	v_fma_f32 v110, v110, v76, v80
	v_fma_f32 v111, v111, v77, v81
	v_exp_f32_e32 v86, v112
	v_exp_f32_e32 v87, v113
	v_exp_f32_e32 v88, v110
	v_exp_f32_e32 v89, v111
	v_add_f32_e32 v86, 1.0, v86
	v_add_f32_e32 v87, 1.0, v87
	v_add_f32_e32 v88, 1.0, v88
	v_add_f32_e32 v89, 1.0, v89
	v_rcp_f32_e32 v86, v86
	v_rcp_f32_e32 v87, v87
	v_rcp_f32_e32 v88, v88
	v_rcp_f32_e32 v89, v89
	v_fma_f32 v86, v86, -2.0, 1.0
	v_fma_f32 v87, v87, -2.0, 1.0
	v_fma_f32 v88, v88, -2.0, 1.0
	v_fma_f32 v89, v89, -2.0, 1.0
	v_mul_f32_e32 v66, v70, v86
	v_mul_f32_e32 v67, v71, v87
	v_mul_f32_e32 v68, v72, v88
	v_mul_f32_e32 v69, v73, v89
	v_cvt_pk_f16_f32 v90, v66, v67
	v_cvt_pk_f16_f32 v91, v68, v69
	v_lshl_add_u32 v93, s54, 8, v99
	s_and_saveexec_b64 s[62:63], s[6:7]
	global_store_dwordx2 v[204:205], v[90:91], off
	ds_write_b64 v93, v[90:91] offset:61440
	s_or_b64 exec, exec, s[62:63]
	s_add_i32 s54, s54, 1
	s_add_i32 s60, s54, 0
	v_mov_b32_e32 v94, s60
	ds_write_b32 v107, v94 offset:61572
	ds_write_b32 v107, v94 offset:61568
	s_cmp_eq_u32 s54, 30
	s_cbranch_scc1 .Lr0_noissue
	global_load_dwordx4 v[132:135], v[196:197], off nt
	global_load_dwordx4 v[136:139], v[196:197], off offset:1024 nt
	global_load_dwordx4 v[140:143], v[196:197], off offset:2048 nt
	global_load_dwordx4 v[144:147], v[196:197], off offset:3072 nt
	global_load_dwordx4 v[148:151], v[198:199], off nt
	global_load_dwordx4 v[152:155], v[198:199], off offset:1024 nt
	global_load_dwordx4 v[156:159], v[198:199], off offset:2048 nt
	global_load_dwordx4 v[160:163], v[198:199], off offset:3072 nt
.Lr0_noissue:
	s_sub_i32 s58, s58, s44
	s_cmp_lg_u32 s54, 30
	s_cbranch_scc1 .Lr0_top
	s_waitcnt vmcnt(0)

.Lr1_gates:
	s_lshl_b32 s60, s58, 13
	s_mov_b32 s61, 0
	v_lshl_add_u64 v[196:197], v[196:197], 0, s[56:57]
	v_lshl_add_u64 v[198:199], v[198:199], 0, s[56:57]
	v_lshl_add_u64 v[200:201], v[200:201], 0, s[56:57]
	v_lshl_add_u64 v[202:203], v[202:203], 0, s[56:57]
	v_lshl_add_u64 v[204:205], v[112:113], 0, s[60:61]
	ds_read_b32 v92, v107 offset:61576
	v_exp_f32_e32 v66, v66
	v_exp_f32_e32 v67, v67
	v_exp_f32_e32 v68, v68
	v_exp_f32_e32 v69, v69
	v_exp_f32_e32 v70, v70
	v_exp_f32_e32 v71, v71
	v_exp_f32_e32 v72, v72
	v_exp_f32_e32 v73, v73
	v_add_f32_e32 v66, 1.0, v66
	v_add_f32_e32 v67, 1.0, v67
	v_add_f32_e32 v68, 1.0, v68
	v_add_f32_e32 v69, 1.0, v69
	v_add_f32_e32 v70, 1.0, v70
	v_add_f32_e32 v71, 1.0, v71
	v_add_f32_e32 v72, 1.0, v72
	v_add_f32_e32 v73, 1.0, v73
	v_rcp_f32_e32 v70, v70
	v_rcp_f32_e32 v71, v71
	v_rcp_f32_e32 v72, v72
	v_rcp_f32_e32 v73, v73
	v_rcp_f32_e32 v74, v66
	v_rcp_f32_e32 v75, v67
	v_rcp_f32_e32 v76, v68
	v_rcp_f32_e32 v77, v69
	v_fma_f32 v70, v100, v70, v102
	v_fma_f32 v71, v100, v71, v102
	v_fma_f32 v72, v100, v72, v102
	v_fma_f32 v73, v100, v73, v102
	v_mul_f32_e32 v78, v74, v70
	v_mul_f32_e32 v79, v75, v71
	v_mul_f32_e32 v80, v76, v72
	v_mul_f32_e32 v81, v77, v73
	v_mov_b32_e32 v82, v78
	v_mov_b32_e32 v83, v79
	v_mov_b32_e32 v84, v80
	v_mov_b32_e32 v85, v81
	v_permlane32_swap_b32_e32 v78, v82
	v_permlane32_swap_b32_e32 v79, v83
	v_permlane32_swap_b32_e32 v80, v84
	v_permlane32_swap_b32_e32 v81, v85
	v_fma_f32 v116, v116, v74, v78
	v_fma_f32 v117, v117, v75, v79
	v_fma_f32 v114, v114, v76, v80
	v_fma_f32 v115, v115, v77, v81
	v_exp_f32_e32 v86, v116
	v_exp_f32_e32 v87, v117
	v_exp_f32_e32 v88, v114
	v_exp_f32_e32 v89, v115
	v_add_f32_e32 v86, 1.0, v86
	v_add_f32_e32 v87, 1.0, v87
	v_add_f32_e32 v88, 1.0, v88
	v_add_f32_e32 v89, 1.0, v89
	v_rcp_f32_e32 v86, v86
	v_rcp_f32_e32 v87, v87
	v_rcp_f32_e32 v88, v88
	v_rcp_f32_e32 v89, v89
	v_fma_f32 v86, v86, -2.0, 1.0
	v_fma_f32 v87, v87, -2.0, 1.0
	v_fma_f32 v88, v88, -2.0, 1.0
	v_fma_f32 v89, v89, -2.0, 1.0
	v_mul_f32_e32 v66, v70, v86
	v_mul_f32_e32 v67, v71, v87
	v_mul_f32_e32 v68, v72, v88
	v_mul_f32_e32 v69, v73, v89
	v_cvt_pk_f16_f32 v90, v66, v67
	v_cvt_pk_f16_f32 v91, v68, v69
	v_lshl_add_u32 v93, s54, 8, v99
	s_waitcnt lgkmcnt(0)
	v_cmp_lt_i32_e32 vcc, s54, v92
	s_cbranch_vccnz .Lr1_pubok

.Lr1_pubok:
	s_and_saveexec_b64 s[62:63], s[6:7]
	global_store_dwordx2 v[204:205], v[90:91], off
	ds_write_b64 v93, v[90:91] offset:61440
	s_or_b64 exec, exec, s[62:63]
	s_add_i32 s54, s54, 1
	s_add_i32 s60, s54, 30
	v_mov_b32_e32 v94, s60
	ds_write_b32 v107, v94 offset:61572
	ds_write_b32 v107, v94 offset:61568
	v_add_f32_e32 v108, v108, v66
	v_add_f32_e32 v110, v110, v68
	v_add_f32_e32 v109, v109, v67
	v_add_f32_e32 v111, v111, v69
	s_cmp_eq_u32 s54, 30
	s_cbranch_scc1 .Lr1_noissue
	global_load_dwordx4 v[132:135], v[196:197], off nt
	global_load_dwordx4 v[136:139], v[196:197], off offset:1024 nt
	global_load_dwordx4 v[140:143], v[196:197], off offset:2048 nt
	global_load_dwordx4 v[144:147], v[196:197], off offset:3072 nt
	global_load_dwordx4 v[148:151], v[198:199], off nt
	global_load_dwordx4 v[152:155], v[198:199], off offset:1024 nt
	global_load_dwordx4 v[156:159], v[198:199], off offset:2048 nt
	global_load_dwordx4 v[160:163], v[198:199], off offset:3072 nt
